# mLSTM carry scan: rolling prefetch (one-dword touch loads two steps ahead into L2, 14 per step) with the step's counted vmcnt waits raised by 14; on top of v9_prohoist
# speedup vs baseline: 1.0027x; 1.0027x over previous
.LBB0_963:
	s_lshl_b32 s0, s20, 9
	s_and_b32 s0, s0, 0xe00
	v_add_u32_e32 v4, s0, v2
	s_bfe_u32 s30, s20, 0x10003
	s_ashr_i32 s0, s20, 4
	s_cmp_eq_u32 s30, 0
	v_ashrrev_i32_e32 v5, 31, v4
	v_cmp_gt_i32_e64 s[38:39], 64, v4
	s_mov_b32 s12, 0
	s_cselect_b64 s[4:5], -1, 0
	s_mul_hi_i32 s25, s0, 0x42
	s_mul_i32 s26, s0, 0x42
	v_lshl_add_u64 v[6:7], v[4:5], 1, s[2:3]
	v_cmp_eq_u32_e64 s[40:41], 0, v4
	s_mov_b32 s27, 57
	s_waitcnt vmcnt(0)
	v_mov_b32_e32 v74, 0
	v_mov_b32_e32 v44, 0
	v_mov_b32_e32 v46, 0
	s_mov_b32 vcc_lo, -11
	s_add_i32 vcc_hi, vcc_lo, 22
	s_min_i32 vcc_hi, vcc_hi, 55
	s_sub_i32 vcc_lo, 35, vcc_lo
	s_max_i32 vcc_lo, vcc_lo, 2
	s_cmp_eq_u32 s30, 0
	s_cselect_b32 vcc_lo, vcc_hi, vcc_lo
	s_add_i32 vcc_lo, vcc_lo, s26
	s_lshl_b32 vcc_lo, vcc_lo, 1
	s_or_b32 vcc_lo, vcc_lo, s30
	s_lshl_b32 s0, vcc_lo, 4
	s_add_u32 s0, s23, s0
	s_addc_u32 s1, s24, 0
	v_and_b32_e32 v80, 15, v2
	v_min_u32_e32 v80, 10, v80
	v_lshlrev_b32_e32 v80, 5, v80
	global_load_dword v84, v80, s[0:1]
	s_mul_i32 s0, vcc_lo, 0x4100
	s_add_u32 s0, s21, s0
	s_addc_u32 s1, s22, 0
	v_lshrrev_b32_e32 v81, 6, v2
	v_and_b32_e32 v82, 63, v2
	v_lshlrev_b32_e32 v82, 2, v82
	v_add_u32_e32 v82, 0x4000, v82
	v_mul_u32_u24_e32 v83, 0x8200, v81
	v_add_u32_e32 v83, v83, v82
	global_load_dword v84, v83, s[0:1]
	v_add_u32_e32 v81, 8, v81
	v_min_u32_e32 v81, 10, v81
	v_mul_u32_u24_e32 v83, 0x8200, v81
	v_add_u32_e32 v83, v83, v82
	global_load_dword v84, v83, s[0:1]
	v_lshlrev_b32_e32 v85, 2, v4
	global_load_dword v84, v85, s[0:1]
	s_add_u32 s0, s0, 0x8200
	s_addc_u32 s1, s1, 0
	global_load_dword v84, v85, s[0:1]
	s_add_u32 s0, s0, 0x8200
	s_addc_u32 s1, s1, 0
	global_load_dword v84, v85, s[0:1]
	s_add_u32 s0, s0, 0x8200
	s_addc_u32 s1, s1, 0
	global_load_dword v84, v85, s[0:1]
	s_add_u32 s0, s0, 0x8200
	s_addc_u32 s1, s1, 0
	global_load_dword v84, v85, s[0:1]
	s_add_u32 s0, s0, 0x8200
	s_addc_u32 s1, s1, 0
	global_load_dword v84, v85, s[0:1]
	s_add_u32 s0, s0, 0x8200
	s_addc_u32 s1, s1, 0
	global_load_dword v84, v85, s[0:1]
	s_add_u32 s0, s0, 0x8200
	s_addc_u32 s1, s1, 0
	global_load_dword v84, v85, s[0:1]
	s_add_u32 s0, s0, 0x8200
	s_addc_u32 s1, s1, 0
	global_load_dword v84, v85, s[0:1]
	s_add_u32 s0, s0, 0x8200
	s_addc_u32 s1, s1, 0
	global_load_dword v84, v85, s[0:1]
	s_add_u32 s0, s0, 0x8200
	s_addc_u32 s1, s1, 0
	global_load_dword v84, v85, s[0:1]
	s_branch .LBB0_965
.LBB0_964:
	s_or_b64 exec, exec, s[0:1]
	s_waitcnt vmcnt(25)
	v_add_f32_e32 v11, v16, v11
	v_max_f32_e32 v12, v10, v10
	v_max_f32_e32 v74, v11, v12
	v_sub_f32_e32 v11, v11, v74
	v_mul_f32_e32 v12, 0x3fb8aa3b, v11
	v_fma_f32 v13, v11, s37, -v12
	v_rndne_f32_e32 v16, v12
	v_fmac_f32_e32 v13, 0x32a5705f, v11
	v_sub_f32_e32 v12, v12, v16
	v_add_f32_e32 v12, v12, v13
	v_exp_f32_e32 v12, v12
	v_cvt_i32_f32_e32 v13, v16
	v_cmp_ngt_f32_e32 vcc, s97, v11
	v_sub_f32_e32 v10, v10, v74
	s_add_i32 s27, s27, -11
	v_ldexp_f32 v12, v12, v13
	v_cndmask_b32_e32 v12, 0, v12, vcc
	v_cmp_nlt_f32_e32 vcc, s10, v11
	v_mul_f32_e32 v11, 0x3fb8aa3b, v10
	v_fma_f32 v13, v10, s37, -v11
	v_rndne_f32_e32 v16, v11
	v_fmac_f32_e32 v13, 0x32a5705f, v10
	v_sub_f32_e32 v11, v11, v16
	v_add_f32_e32 v11, v11, v13
	v_exp_f32_e32 v11, v11
	v_cvt_i32_f32_e32 v13, v16
	v_cndmask_b32_e32 v12, v210, v12, vcc
	v_cmp_ngt_f32_e32 vcc, s97, v10
	s_add_i32 s0, s80, -10
	v_ldexp_f32 v11, v11, v13
	v_cndmask_b32_e32 v11, 0, v11, vcc
	v_cmp_nlt_f32_e32 vcc, s10, v10
	s_add_i32 s12, s80, 1
	s_cmp_gt_u32 s0, 54
	v_cndmask_b32_e32 v10, v210, v11, vcc
	v_pk_mul_f32 v[8:9], v[8:9], v[10:11] op_sel_hi:[1,0]
	s_nop 0
	v_pk_fma_f32 v[44:45], v[14:15], v[12:13], v[8:9] op_sel_hi:[1,0,1]
	s_nop 0
	v_mov_b32_e32 v46, v45
	s_cbranch_scc1 .LBB0_962

.LBB0_987:
	s_or_b64 exec, exec, s[0:1]
	s_sub_i32 vcc_lo, 57, s27
	s_add_i32 vcc_hi, vcc_lo, 22
	s_min_i32 vcc_hi, vcc_hi, 55
	s_sub_i32 vcc_lo, 35, vcc_lo
	s_max_i32 vcc_lo, vcc_lo, 2
	s_cmp_eq_u32 s30, 0
	s_cselect_b32 vcc_lo, vcc_hi, vcc_lo
	s_add_i32 vcc_lo, vcc_lo, s26
	s_lshl_b32 vcc_lo, vcc_lo, 1
	s_or_b32 vcc_lo, vcc_lo, s30
	s_lshl_b32 s0, vcc_lo, 4
	s_add_u32 s0, s23, s0
	s_addc_u32 s1, s24, 0
	v_and_b32_e32 v80, 15, v2
	v_min_u32_e32 v80, 10, v80
	v_lshlrev_b32_e32 v80, 5, v80
	global_load_dword v84, v80, s[0:1]
	s_mul_i32 s0, vcc_lo, 0x4100
	s_add_u32 s0, s21, s0
	s_addc_u32 s1, s22, 0
	v_lshrrev_b32_e32 v81, 6, v2
	v_and_b32_e32 v82, 63, v2
	v_lshlrev_b32_e32 v82, 2, v82
	v_add_u32_e32 v82, 0x4000, v82
	v_mul_u32_u24_e32 v83, 0x8200, v81
	v_add_u32_e32 v83, v83, v82
	global_load_dword v84, v83, s[0:1]
	v_add_u32_e32 v81, 8, v81
	v_min_u32_e32 v81, 10, v81
	v_mul_u32_u24_e32 v83, 0x8200, v81
	v_add_u32_e32 v83, v83, v82
	global_load_dword v84, v83, s[0:1]
	v_lshlrev_b32_e32 v85, 2, v4
	global_load_dword v84, v85, s[0:1]
	s_add_u32 s0, s0, 0x8200
	s_addc_u32 s1, s1, 0
	global_load_dword v84, v85, s[0:1]
	s_add_u32 s0, s0, 0x8200
	s_addc_u32 s1, s1, 0
	global_load_dword v84, v85, s[0:1]
	s_add_u32 s0, s0, 0x8200
	s_addc_u32 s1, s1, 0
	global_load_dword v84, v85, s[0:1]
	s_add_u32 s0, s0, 0x8200
	s_addc_u32 s1, s1, 0
	global_load_dword v84, v85, s[0:1]
	s_add_u32 s0, s0, 0x8200
	s_addc_u32 s1, s1, 0
	global_load_dword v84, v85, s[0:1]
	s_add_u32 s0, s0, 0x8200
	s_addc_u32 s1, s1, 0
	global_load_dword v84, v85, s[0:1]
	s_add_u32 s0, s0, 0x8200
	s_addc_u32 s1, s1, 0
	global_load_dword v84, v85, s[0:1]
	s_add_u32 s0, s0, 0x8200
	s_addc_u32 s1, s1, 0
	global_load_dword v84, v85, s[0:1]
	s_add_u32 s0, s0, 0x8200
	s_addc_u32 s1, s1, 0
	global_load_dword v84, v85, s[0:1]
	s_add_u32 s0, s0, 0x8200
	s_addc_u32 s1, s1, 0
	global_load_dword v84, v85, s[0:1]
	v_bfe_u32 v77, v46, 16, 1
	s_lshl_b64 s[0:1], s[78:79], 13
	v_add3_u32 v77, v46, v77, s29
	v_lshl_add_u64 v[78:79], v[6:7], 0, s[0:1]
	global_store_short_d16_hi v[78:79], v77, off
	s_and_saveexec_b64 s[0:1], s[38:39]
	s_cbranch_execz .LBB0_989
	v_add_co_u32_e32 v56, vcc, 0x4000, v56
	s_nop 1
	v_addc_co_u32_e32 v57, vcc, 0, v57, vcc
	global_store_dword v[56:57], v44, off

.LBB0_991:
	s_or_b64 exec, exec, s[0:1]
	s_waitcnt vmcnt(35)
	v_add_f32_e32 v56, v74, v55
	v_max_f32_e32 v55, v54, v54
	v_max_f32_e32 v55, v56, v55
	v_sub_f32_e32 v56, v56, v55
	v_mul_f32_e32 v57, 0x3fb8aa3b, v56
	v_fma_f32 v74, v56, s37, -v57
	v_rndne_f32_e32 v77, v57
	v_fmac_f32_e32 v74, 0x32a5705f, v56
	v_sub_f32_e32 v57, v57, v77
	v_add_f32_e32 v57, v57, v74
	v_exp_f32_e32 v57, v57
	v_cvt_i32_f32_e32 v74, v77
	v_cmp_ngt_f32_e32 vcc, s97, v56
	v_sub_f32_e32 v54, v54, v55
	s_lshl_b64 s[0:1], s[74:75], 13
	v_ldexp_f32 v57, v57, v74
	v_cndmask_b32_e32 v57, 0, v57, vcc
	v_cmp_nlt_f32_e32 vcc, s10, v56
	s_nop 1
	v_cndmask_b32_e32 v56, v210, v57, vcc
	v_mul_f32_e32 v57, 0x3fb8aa3b, v54
	v_fma_f32 v74, v54, s37, -v57
	v_rndne_f32_e32 v77, v57
	v_fmac_f32_e32 v74, 0x32a5705f, v54
	v_sub_f32_e32 v57, v57, v77
	v_add_f32_e32 v57, v57, v74
	v_exp_f32_e32 v57, v57
	v_cvt_i32_f32_e32 v74, v77
	v_cmp_ngt_f32_e32 vcc, s97, v54
	v_ldexp_f32 v57, v57, v74
	s_nop 0
	v_cndmask_b32_e32 v57, 0, v57, vcc
	v_cmp_nlt_f32_e32 vcc, s10, v54
	s_nop 1
	v_cndmask_b32_e32 v57, v210, v57, vcc
	v_mul_f32_e32 v54, v47, v57
	v_pk_fma_f32 v[46:47], v[46:47], v[56:57], v[54:55] op_sel_hi:[1,1,0]
	v_mul_f32_e32 v54, v57, v76
	v_fmac_f32_e32 v54, v44, v56
	v_bfe_u32 v44, v46, 16, 1
	v_add3_u32 v44, v46, v44, s29
	v_lshl_add_u64 v[56:57], v[6:7], 0, s[0:1]
	global_store_short_d16_hi v[56:57], v44, off
	s_and_saveexec_b64 s[0:1], s[38:39]
	s_cbranch_execz .LBB0_993
	v_add_co_u32_e32 v52, vcc, 0x4000, v52
	s_nop 1
	v_addc_co_u32_e32 v53, vcc, 0, v53, vcc
	global_store_dword v[52:53], v54, off

.LBB0_995:
	s_or_b64 exec, exec, s[0:1]
	s_waitcnt vmcnt(34)
	v_add_f32_e32 v44, v55, v51
	v_max_f32_e32 v47, v50, v50
	v_max_f32_e32 v51, v44, v47
	v_sub_f32_e32 v44, v44, v51
	v_mul_f32_e32 v47, 0x3fb8aa3b, v44
	v_fma_f32 v52, v44, s37, -v47
	v_rndne_f32_e32 v53, v47
	v_fmac_f32_e32 v52, 0x32a5705f, v44
	v_sub_f32_e32 v47, v47, v53
	v_add_f32_e32 v47, v47, v52
	v_exp_f32_e32 v47, v47
	v_cvt_i32_f32_e32 v52, v53
	v_cmp_ngt_f32_e32 vcc, s97, v44
	s_lshl_b64 s[0:1], s[70:71], 13
	v_ldexp_f32 v47, v47, v52
	v_cndmask_b32_e32 v47, 0, v47, vcc
	v_cmp_nlt_f32_e32 vcc, s10, v44
	v_sub_f32_e32 v44, v50, v51
	s_nop 0
	v_cndmask_b32_e32 v52, v210, v47, vcc
	v_mul_f32_e32 v47, 0x3fb8aa3b, v44
	v_fma_f32 v50, v44, s37, -v47
	v_rndne_f32_e32 v53, v47
	v_fmac_f32_e32 v50, 0x32a5705f, v44
	v_sub_f32_e32 v47, v47, v53
	v_add_f32_e32 v47, v47, v50
	v_exp_f32_e32 v47, v47
	v_cvt_i32_f32_e32 v50, v53
	v_cmp_ngt_f32_e32 vcc, s97, v44
	v_ldexp_f32 v47, v47, v50
	s_nop 0
	v_cndmask_b32_e32 v47, 0, v47, vcc
	v_cmp_nlt_f32_e32 vcc, s10, v44
	s_nop 1
	v_cndmask_b32_e32 v53, v210, v47, vcc
	v_mov_b32_e32 v47, v45
	v_mul_f32_e32 v44, v45, v53
	v_pk_fma_f32 v[44:45], v[46:47], v[52:53], v[44:45] op_sel_hi:[1,1,0]
	v_mul_f32_e32 v46, v53, v75
	v_bfe_u32 v45, v44, 16, 1
	v_fmac_f32_e32 v46, v54, v52
	v_add3_u32 v45, v44, v45, s29
	v_lshl_add_u64 v[52:53], v[6:7], 0, s[0:1]
	global_store_short_d16_hi v[52:53], v45, off
	s_and_saveexec_b64 s[0:1], s[38:39]
	s_cbranch_execz .LBB0_997
	v_add_co_u32_e32 v48, vcc, 0x4000, v48
	s_nop 1
	v_addc_co_u32_e32 v49, vcc, 0, v49, vcc
	global_store_dword v[48:49], v46, off

.LBB0_999:
	s_or_b64 exec, exec, s[0:1]
	s_waitcnt vmcnt(33)
	v_add_f32_e32 v43, v51, v43
	v_max_f32_e32 v45, v42, v42
	v_max_f32_e32 v47, v43, v45
	v_sub_f32_e32 v43, v43, v47
	v_mul_f32_e32 v45, 0x3fb8aa3b, v43
	v_fma_f32 v48, v43, s37, -v45
	v_rndne_f32_e32 v49, v45
	v_fmac_f32_e32 v48, 0x32a5705f, v43
	v_sub_f32_e32 v45, v45, v49
	v_add_f32_e32 v45, v45, v48
	v_exp_f32_e32 v45, v45
	v_cvt_i32_f32_e32 v48, v49
	v_cmp_ngt_f32_e32 vcc, s97, v43
	v_sub_f32_e32 v42, v42, v47
	s_lshl_b64 s[0:1], s[66:67], 13
	v_ldexp_f32 v45, v45, v48
	v_cndmask_b32_e32 v45, 0, v45, vcc
	v_cmp_nlt_f32_e32 vcc, s10, v43
	v_mul_f32_e32 v43, 0x3fb8aa3b, v42
	v_rndne_f32_e32 v49, v43
	v_cndmask_b32_e32 v48, v210, v45, vcc
	v_fma_f32 v45, v42, s37, -v43
	v_fmac_f32_e32 v45, 0x32a5705f, v42
	v_sub_f32_e32 v43, v43, v49
	v_add_f32_e32 v43, v43, v45
	v_exp_f32_e32 v43, v43
	v_cvt_i32_f32_e32 v45, v49
	v_cmp_ngt_f32_e32 vcc, s97, v42
	v_ldexp_f32 v43, v43, v45
	s_nop 0
	v_cndmask_b32_e32 v43, 0, v43, vcc
	v_cmp_nlt_f32_e32 vcc, s10, v42
	v_mov_b32_e32 v45, v73
	s_nop 0
	v_cndmask_b32_e32 v49, v210, v43, vcc
	v_mul_f32_e32 v42, v73, v49
	v_pk_fma_f32 v[42:43], v[44:45], v[48:49], v[42:43] op_sel_hi:[1,1,0]
	v_mul_f32_e32 v44, v49, v72
	v_bfe_u32 v43, v42, 16, 1
	v_fmac_f32_e32 v44, v46, v48
	v_add3_u32 v43, v42, v43, s29
	v_lshl_add_u64 v[48:49], v[6:7], 0, s[0:1]
	global_store_short_d16_hi v[48:49], v43, off
	s_and_saveexec_b64 s[0:1], s[38:39]
	s_cbranch_execz .LBB0_1001
	v_add_co_u32_e32 v40, vcc, 0x4000, v40
	s_nop 1
	v_addc_co_u32_e32 v41, vcc, 0, v41, vcc
	global_store_dword v[40:41], v44, off

.LBB0_1003:
	s_or_b64 exec, exec, s[0:1]
	s_waitcnt vmcnt(32)
	v_add_f32_e32 v39, v47, v39
	v_max_f32_e32 v40, v38, v38
	v_max_f32_e32 v41, v39, v40
	v_sub_f32_e32 v39, v39, v41
	v_mul_f32_e32 v40, 0x3fb8aa3b, v39
	v_fma_f32 v43, v39, s37, -v40
	v_rndne_f32_e32 v45, v40
	v_fmac_f32_e32 v43, 0x32a5705f, v39
	v_sub_f32_e32 v40, v40, v45
	v_add_f32_e32 v40, v40, v43
	v_exp_f32_e32 v40, v40
	v_cvt_i32_f32_e32 v43, v45
	v_cmp_ngt_f32_e32 vcc, s97, v39
	v_sub_f32_e32 v38, v38, v41
	s_lshl_b64 s[0:1], s[62:63], 13
	v_ldexp_f32 v40, v40, v43
	v_cndmask_b32_e32 v40, 0, v40, vcc
	v_cmp_nlt_f32_e32 vcc, s10, v39
	v_mul_f32_e32 v39, 0x3fb8aa3b, v38
	v_rndne_f32_e32 v43, v39
	v_cndmask_b32_e32 v46, v210, v40, vcc
	v_fma_f32 v40, v38, s37, -v39
	v_fmac_f32_e32 v40, 0x32a5705f, v38
	v_sub_f32_e32 v39, v39, v43
	v_add_f32_e32 v39, v39, v40
	v_exp_f32_e32 v39, v39
	v_cvt_i32_f32_e32 v40, v43
	v_cmp_ngt_f32_e32 vcc, s97, v38
	v_mov_b32_e32 v43, v70
	v_ldexp_f32 v39, v39, v40
	v_cndmask_b32_e32 v39, 0, v39, vcc
	v_cmp_nlt_f32_e32 vcc, s10, v38
	s_nop 1
	v_cndmask_b32_e32 v47, v210, v39, vcc
	v_mul_f32_e32 v38, v70, v47
	v_pk_fma_f32 v[38:39], v[42:43], v[46:47], v[38:39] op_sel_hi:[1,1,0]
	v_mul_f32_e32 v40, v47, v71
	v_bfe_u32 v39, v38, 16, 1
	v_fmac_f32_e32 v40, v44, v46
	v_add3_u32 v39, v38, v39, s29
	v_lshl_add_u64 v[42:43], v[6:7], 0, s[0:1]
	global_store_short_d16_hi v[42:43], v39, off
	s_and_saveexec_b64 s[0:1], s[38:39]
	s_cbranch_execz .LBB0_1005
	v_add_co_u32_e32 v36, vcc, 0x4000, v36
	s_nop 1
	v_addc_co_u32_e32 v37, vcc, 0, v37, vcc
	global_store_dword v[36:37], v40, off

.LBB0_1007:
	s_or_b64 exec, exec, s[0:1]
	s_waitcnt vmcnt(31)
	v_add_f32_e32 v35, v41, v35
	v_max_f32_e32 v36, v34, v34
	v_max_f32_e32 v37, v35, v36
	v_sub_f32_e32 v35, v35, v37
	v_mul_f32_e32 v36, 0x3fb8aa3b, v35
	v_fma_f32 v39, v35, s37, -v36
	v_rndne_f32_e32 v41, v36
	v_fmac_f32_e32 v39, 0x32a5705f, v35
	v_sub_f32_e32 v36, v36, v41
	v_add_f32_e32 v36, v36, v39
	v_exp_f32_e32 v36, v36
	v_cvt_i32_f32_e32 v39, v41
	v_cmp_ngt_f32_e32 vcc, s97, v35
	v_sub_f32_e32 v34, v34, v37
	s_lshl_b64 s[0:1], s[58:59], 13
	v_ldexp_f32 v36, v36, v39
	v_cndmask_b32_e32 v36, 0, v36, vcc
	v_cmp_nlt_f32_e32 vcc, s10, v35
	v_mul_f32_e32 v35, 0x3fb8aa3b, v34
	v_rndne_f32_e32 v39, v35
	v_cndmask_b32_e32 v42, v210, v36, vcc
	v_fma_f32 v36, v34, s37, -v35
	v_fmac_f32_e32 v36, 0x32a5705f, v34
	v_sub_f32_e32 v35, v35, v39
	v_add_f32_e32 v35, v35, v36
	v_exp_f32_e32 v35, v35
	v_cvt_i32_f32_e32 v36, v39
	v_cmp_ngt_f32_e32 vcc, s97, v34
	v_mov_b32_e32 v39, v69
	v_ldexp_f32 v35, v35, v36
	v_cndmask_b32_e32 v35, 0, v35, vcc
	v_cmp_nlt_f32_e32 vcc, s10, v34
	s_nop 1
	v_cndmask_b32_e32 v43, v210, v35, vcc
	v_mul_f32_e32 v34, v69, v43
	v_pk_fma_f32 v[34:35], v[38:39], v[42:43], v[34:35] op_sel_hi:[1,1,0]
	v_mul_f32_e32 v36, v43, v68
	v_bfe_u32 v35, v34, 16, 1
	v_fmac_f32_e32 v36, v40, v42
	v_add3_u32 v35, v34, v35, s29
	v_lshl_add_u64 v[38:39], v[6:7], 0, s[0:1]
	global_store_short_d16_hi v[38:39], v35, off
	s_and_saveexec_b64 s[0:1], s[38:39]
	s_cbranch_execz .LBB0_1009
	v_add_co_u32_e32 v32, vcc, 0x4000, v32
	s_nop 1
	v_addc_co_u32_e32 v33, vcc, 0, v33, vcc
	global_store_dword v[32:33], v36, off

.LBB0_1011:
	s_or_b64 exec, exec, s[0:1]
	s_waitcnt vmcnt(30)
	v_add_f32_e32 v31, v37, v31
	v_max_f32_e32 v32, v30, v30
	v_max_f32_e32 v33, v31, v32
	v_sub_f32_e32 v31, v31, v33
	v_mul_f32_e32 v32, 0x3fb8aa3b, v31
	v_fma_f32 v35, v31, s37, -v32
	v_rndne_f32_e32 v37, v32
	v_fmac_f32_e32 v35, 0x32a5705f, v31
	v_sub_f32_e32 v32, v32, v37
	v_add_f32_e32 v32, v32, v35
	v_exp_f32_e32 v32, v32
	v_cvt_i32_f32_e32 v35, v37
	v_cmp_ngt_f32_e32 vcc, s97, v31
	v_sub_f32_e32 v30, v30, v33
	s_lshl_b64 s[0:1], s[54:55], 13
	v_ldexp_f32 v32, v32, v35
	v_cndmask_b32_e32 v32, 0, v32, vcc
	v_cmp_nlt_f32_e32 vcc, s10, v31
	v_mul_f32_e32 v31, 0x3fb8aa3b, v30
	v_rndne_f32_e32 v35, v31
	v_cndmask_b32_e32 v38, v210, v32, vcc
	v_fma_f32 v32, v30, s37, -v31
	v_fmac_f32_e32 v32, 0x32a5705f, v30
	v_sub_f32_e32 v31, v31, v35
	v_add_f32_e32 v31, v31, v32
	v_exp_f32_e32 v31, v31
	v_cvt_i32_f32_e32 v32, v35
	v_cmp_ngt_f32_e32 vcc, s97, v30
	v_mov_b32_e32 v35, v66
	v_ldexp_f32 v31, v31, v32
	v_cndmask_b32_e32 v31, 0, v31, vcc
	v_cmp_nlt_f32_e32 vcc, s10, v30
	s_nop 1
	v_cndmask_b32_e32 v39, v210, v31, vcc
	v_mul_f32_e32 v30, v66, v39
	v_pk_fma_f32 v[30:31], v[34:35], v[38:39], v[30:31] op_sel_hi:[1,1,0]
	v_mul_f32_e32 v32, v39, v67
	v_bfe_u32 v31, v30, 16, 1
	v_fmac_f32_e32 v32, v36, v38
	v_add3_u32 v31, v30, v31, s29
	v_lshl_add_u64 v[34:35], v[6:7], 0, s[0:1]
	global_store_short_d16_hi v[34:35], v31, off
	s_and_saveexec_b64 s[0:1], s[38:39]
	s_cbranch_execz .LBB0_1013
	v_add_co_u32_e32 v28, vcc, 0x4000, v28
	s_nop 1
	v_addc_co_u32_e32 v29, vcc, 0, v29, vcc
	global_store_dword v[28:29], v32, off

.LBB0_1015:
	s_or_b64 exec, exec, s[0:1]
	s_waitcnt vmcnt(29)
	v_add_f32_e32 v27, v33, v27
	v_max_f32_e32 v28, v26, v26
	v_max_f32_e32 v29, v27, v28
	v_sub_f32_e32 v27, v27, v29
	v_mul_f32_e32 v28, 0x3fb8aa3b, v27
	v_fma_f32 v31, v27, s37, -v28
	v_rndne_f32_e32 v33, v28
	v_fmac_f32_e32 v31, 0x32a5705f, v27
	v_sub_f32_e32 v28, v28, v33
	v_add_f32_e32 v28, v28, v31
	v_exp_f32_e32 v28, v28
	v_cvt_i32_f32_e32 v31, v33
	v_cmp_ngt_f32_e32 vcc, s97, v27
	v_sub_f32_e32 v26, v26, v29
	s_lshl_b64 s[0:1], s[50:51], 13
	v_ldexp_f32 v28, v28, v31
	v_cndmask_b32_e32 v28, 0, v28, vcc
	v_cmp_nlt_f32_e32 vcc, s10, v27
	v_mul_f32_e32 v27, 0x3fb8aa3b, v26
	v_rndne_f32_e32 v31, v27
	v_cndmask_b32_e32 v34, v210, v28, vcc
	v_fma_f32 v28, v26, s37, -v27
	v_fmac_f32_e32 v28, 0x32a5705f, v26
	v_sub_f32_e32 v27, v27, v31
	v_add_f32_e32 v27, v27, v28
	v_exp_f32_e32 v27, v27
	v_cvt_i32_f32_e32 v28, v31
	v_cmp_ngt_f32_e32 vcc, s97, v26
	v_mov_b32_e32 v31, v65
	v_ldexp_f32 v27, v27, v28
	v_cndmask_b32_e32 v27, 0, v27, vcc
	v_cmp_nlt_f32_e32 vcc, s10, v26
	s_nop 1
	v_cndmask_b32_e32 v35, v210, v27, vcc
	v_mul_f32_e32 v26, v65, v35
	v_pk_fma_f32 v[26:27], v[30:31], v[34:35], v[26:27] op_sel_hi:[1,1,0]
	v_mul_f32_e32 v28, v35, v64
	v_bfe_u32 v27, v26, 16, 1
	v_fmac_f32_e32 v28, v32, v34
	v_add3_u32 v27, v26, v27, s29
	v_lshl_add_u64 v[30:31], v[6:7], 0, s[0:1]
	global_store_short_d16_hi v[30:31], v27, off
	s_and_saveexec_b64 s[0:1], s[38:39]
	s_cbranch_execz .LBB0_1017
	v_add_co_u32_e32 v24, vcc, 0x4000, v24
	s_nop 1
	v_addc_co_u32_e32 v25, vcc, 0, v25, vcc
	global_store_dword v[24:25], v28, off

.LBB0_1019:
	s_or_b64 exec, exec, s[0:1]
	s_waitcnt vmcnt(28)
	v_add_f32_e32 v23, v29, v23
	v_max_f32_e32 v24, v22, v22
	v_max_f32_e32 v25, v23, v24
	v_sub_f32_e32 v23, v23, v25
	v_mul_f32_e32 v24, 0x3fb8aa3b, v23
	v_fma_f32 v27, v23, s37, -v24
	v_rndne_f32_e32 v29, v24
	v_fmac_f32_e32 v27, 0x32a5705f, v23
	v_sub_f32_e32 v24, v24, v29
	v_add_f32_e32 v24, v24, v27
	v_exp_f32_e32 v24, v24
	v_cvt_i32_f32_e32 v27, v29
	v_cmp_ngt_f32_e32 vcc, s97, v23
	v_sub_f32_e32 v22, v22, v25
	s_lshl_b64 s[0:1], s[46:47], 13
	v_ldexp_f32 v24, v24, v27
	v_cndmask_b32_e32 v24, 0, v24, vcc
	v_cmp_nlt_f32_e32 vcc, s10, v23
	v_mul_f32_e32 v23, 0x3fb8aa3b, v22
	v_rndne_f32_e32 v27, v23
	v_cndmask_b32_e32 v30, v210, v24, vcc
	v_fma_f32 v24, v22, s37, -v23
	v_fmac_f32_e32 v24, 0x32a5705f, v22
	v_sub_f32_e32 v23, v23, v27
	v_add_f32_e32 v23, v23, v24
	v_exp_f32_e32 v23, v23
	v_cvt_i32_f32_e32 v24, v27
	v_cmp_ngt_f32_e32 vcc, s97, v22
	v_mov_b32_e32 v27, v62
	v_ldexp_f32 v23, v23, v24
	v_cndmask_b32_e32 v23, 0, v23, vcc
	v_cmp_nlt_f32_e32 vcc, s10, v22
	s_nop 1
	v_cndmask_b32_e32 v31, v210, v23, vcc
	v_mul_f32_e32 v22, v62, v31
	v_pk_fma_f32 v[22:23], v[26:27], v[30:31], v[22:23] op_sel_hi:[1,1,0]
	v_mul_f32_e32 v24, v31, v63
	v_bfe_u32 v23, v22, 16, 1
	v_fmac_f32_e32 v24, v28, v30
	v_add3_u32 v23, v22, v23, s29
	v_lshl_add_u64 v[26:27], v[6:7], 0, s[0:1]
	global_store_short_d16_hi v[26:27], v23, off
	s_and_saveexec_b64 s[0:1], s[38:39]
	s_cbranch_execz .LBB0_1021
	v_add_co_u32_e32 v20, vcc, 0x4000, v20
	s_nop 1
	v_addc_co_u32_e32 v21, vcc, 0, v21, vcc
	global_store_dword v[20:21], v24, off

.LBB0_1023:
	s_or_b64 exec, exec, s[0:1]
	s_waitcnt vmcnt(27)
	v_add_f32_e32 v19, v25, v19
	v_max_f32_e32 v20, v18, v18
	v_max_f32_e32 v21, v19, v20
	v_sub_f32_e32 v19, v19, v21
	v_mul_f32_e32 v20, 0x3fb8aa3b, v19
	v_fma_f32 v23, v19, s37, -v20
	v_rndne_f32_e32 v25, v20
	v_fmac_f32_e32 v23, 0x32a5705f, v19
	v_sub_f32_e32 v20, v20, v25
	v_add_f32_e32 v20, v20, v23
	v_exp_f32_e32 v20, v20
	v_cvt_i32_f32_e32 v23, v25
	v_cmp_ngt_f32_e32 vcc, s97, v19
	v_sub_f32_e32 v18, v18, v21
	s_lshl_b64 s[0:1], s[42:43], 13
	v_ldexp_f32 v20, v20, v23
	v_cndmask_b32_e32 v20, 0, v20, vcc
	v_cmp_nlt_f32_e32 vcc, s10, v19
	v_mul_f32_e32 v19, 0x3fb8aa3b, v18
	v_rndne_f32_e32 v23, v19
	v_cndmask_b32_e32 v26, v210, v20, vcc
	v_fma_f32 v20, v18, s37, -v19
	v_fmac_f32_e32 v20, 0x32a5705f, v18
	v_sub_f32_e32 v19, v19, v23
	v_add_f32_e32 v19, v19, v20
	v_exp_f32_e32 v19, v19
	v_cvt_i32_f32_e32 v20, v23
	v_cmp_ngt_f32_e32 vcc, s97, v18
	v_mov_b32_e32 v23, v61
	v_ldexp_f32 v19, v19, v20
	v_cndmask_b32_e32 v19, 0, v19, vcc
	v_cmp_nlt_f32_e32 vcc, s10, v18
	s_nop 1
	v_cndmask_b32_e32 v27, v210, v19, vcc
	v_mul_f32_e32 v18, v61, v27
	v_pk_fma_f32 v[18:19], v[22:23], v[26:27], v[18:19] op_sel_hi:[1,1,0]
	v_mul_f32_e32 v20, v27, v60
	v_bfe_u32 v19, v18, 16, 1
	v_fmac_f32_e32 v20, v24, v26
	v_add3_u32 v19, v18, v19, s29
	v_lshl_add_u64 v[22:23], v[6:7], 0, s[0:1]
	global_store_short_d16_hi v[22:23], v19, off
	s_and_saveexec_b64 s[0:1], s[38:39]
	s_cbranch_execz .LBB0_1025
	v_add_co_u32_e32 v16, vcc, 0x4000, v16
	s_nop 1
	v_addc_co_u32_e32 v17, vcc, 0, v17, vcc
	global_store_dword v[16:17], v20, off

.LBB0_1027:
	s_or_b64 exec, exec, s[0:1]
	s_waitcnt vmcnt(26)
	v_add_f32_e32 v15, v21, v15
	v_max_f32_e32 v16, v14, v14
	v_max_f32_e32 v16, v15, v16
	v_sub_f32_e32 v15, v15, v16
	v_mul_f32_e32 v17, 0x3fb8aa3b, v15
	v_fma_f32 v19, v15, s37, -v17
	v_rndne_f32_e32 v21, v17
	v_fmac_f32_e32 v19, 0x32a5705f, v15
	v_sub_f32_e32 v17, v17, v21
	v_add_f32_e32 v17, v17, v19
	v_exp_f32_e32 v17, v17
	v_cvt_i32_f32_e32 v19, v21
	v_cmp_ngt_f32_e32 vcc, s97, v15
	v_sub_f32_e32 v14, v14, v16
	s_lshl_b64 s[0:1], s[14:15], 13
	v_ldexp_f32 v17, v17, v19
	v_cndmask_b32_e32 v17, 0, v17, vcc
	v_cmp_nlt_f32_e32 vcc, s10, v15
	v_mul_f32_e32 v15, 0x3fb8aa3b, v14
	v_rndne_f32_e32 v19, v15
	v_cndmask_b32_e32 v22, v210, v17, vcc
	v_fma_f32 v17, v14, s37, -v15
	v_fmac_f32_e32 v17, 0x32a5705f, v14
	v_sub_f32_e32 v15, v15, v19
	v_add_f32_e32 v15, v15, v17
	v_exp_f32_e32 v15, v15
	v_cvt_i32_f32_e32 v17, v19
	v_cmp_ngt_f32_e32 vcc, s97, v14
	v_mov_b32_e32 v19, v58
	v_ldexp_f32 v15, v15, v17
	v_cndmask_b32_e32 v15, 0, v15, vcc
	v_cmp_nlt_f32_e32 vcc, s10, v14
	s_nop 1
	v_cndmask_b32_e32 v23, v210, v15, vcc
	v_pk_mul_f32 v[14:15], v[18:19], v[22:23]
	v_mul_f32_e32 v18, v20, v22
	v_mul_f32_e32 v20, v23, v59
	v_mov_b32_e32 v19, v14
	v_mov_b32_e32 v21, v15
	v_pk_add_f32 v[14:15], v[18:19], v[20:21]
	v_lshl_add_u64 v[18:19], v[6:7], 0, s[0:1]
	v_bfe_u32 v17, v15, 16, 1
	v_add3_u32 v17, v15, v17, s29
	global_store_short_d16_hi v[18:19], v17, off
	s_and_saveexec_b64 s[0:1], s[38:39]
	s_cbranch_execz .LBB0_1029
	v_add_co_u32_e32 v12, vcc, 0x4000, v12
	s_nop 1
	v_addc_co_u32_e32 v13, vcc, 0, v13, vcc
	global_store_dword v[12:13], v14, off
